# conv_ffn: wait for prefetched block moved after processing (vmcnt counted), on top of v28
# speedup vs baseline: 1.0010x; 1.0010x over previous
.LBB0_68:
	s_waitcnt vmcnt(8)
	s_andn2_b64 vcc, exec, s[0:1]
	s_cbranch_vccnz .Lcf_hna
	s_waitcnt vmcnt(0)
.Lcf_hna:
	v_pk_mul_f32 v[2:3], v[2:3], s[8:9] op_sel_hi:[1,0]
	ds_write2_b32 v75, v2, v3 offset1:1
	v_pk_mul_f32 v[2:3], v[4:5], s[8:9] op_sel_hi:[1,0]
	ds_write2_b32 v75, v2, v3 offset0:2 offset1:3
	v_pk_mul_f32 v[2:3], v[6:7], s[8:9] op_sel_hi:[1,0]
	v_add_u32_e32 v4, 0x420, v75
	ds_write2_b32 v4, v2, v3 offset1:1
	v_pk_mul_f32 v[2:3], v[8:9], s[8:9] op_sel_hi:[1,0]
	v_add_u32_e32 v4, 0x428, v75
	ds_write2_b32 v4, v2, v3 offset1:1
	v_pk_mul_f32 v[2:3], v[10:11], s[8:9] op_sel_hi:[1,0]
	v_add_u32_e32 v4, 0x840, v75
	ds_write2_b32 v4, v2, v3 offset1:1
	v_pk_mul_f32 v[2:3], v[12:13], s[8:9] op_sel_hi:[1,0]
	v_add_u32_e32 v4, 0x848, v75
	ds_write2_b32 v4, v2, v3 offset1:1
	v_pk_mul_f32 v[2:3], v[14:15], s[8:9] op_sel_hi:[1,0]
	v_add_u32_e32 v4, 0xc60, v75
	ds_write2_b32 v4, v2, v3 offset1:1
	v_pk_mul_f32 v[2:3], v[16:17], s[8:9] op_sel_hi:[1,0]
	v_add_u32_e32 v4, 0xc68, v75
	ds_write2_b32 v4, v2, v3 offset1:1
	v_pk_mul_f32 v[2:3], v[18:19], s[8:9] op_sel_hi:[1,0]
	v_add_u32_e32 v4, 0x1080, v75
	ds_write2_b32 v4, v2, v3 offset1:1
	v_pk_mul_f32 v[2:3], v[20:21], s[8:9] op_sel_hi:[1,0]
	v_add_u32_e32 v4, 0x1088, v75
	ds_write2_b32 v4, v2, v3 offset1:1
	v_pk_mul_f32 v[2:3], v[22:23], s[8:9] op_sel_hi:[1,0]
	v_add_u32_e32 v4, 0x14a0, v75
	ds_write2_b32 v4, v2, v3 offset1:1
	v_pk_mul_f32 v[2:3], v[24:25], s[8:9] op_sel_hi:[1,0]
	v_add_u32_e32 v4, 0x14a8, v75
	ds_write2_b32 v4, v2, v3 offset1:1
	v_pk_mul_f32 v[2:3], v[26:27], s[8:9] op_sel_hi:[1,0]
	v_add_u32_e32 v4, 0x18c0, v75
	ds_write2_b32 v4, v2, v3 offset1:1
	v_pk_mul_f32 v[2:3], v[28:29], s[8:9] op_sel_hi:[1,0]
	v_add_u32_e32 v4, 0x18c8, v75
	ds_write2_b32 v4, v2, v3 offset1:1
	v_pk_mul_f32 v[2:3], v[30:31], s[8:9] op_sel_hi:[1,0]
	v_add_u32_e32 v4, 0x1ce0, v75
	ds_write2_b32 v4, v2, v3 offset1:1
	v_pk_mul_f32 v[2:3], v[32:33], s[8:9] op_sel_hi:[1,0]
	v_add_u32_e32 v4, 0x1ce8, v75
	ds_write2_b32 v4, v2, v3 offset1:1
	s_waitcnt lgkmcnt(0)
	v_add_u32_e32 v5, 0x400, v73
	ds_read2_b32 v[8:9], v73 offset1:16
	ds_read2_b32 v[10:11], v73 offset0:33 offset1:49
	ds_read2_b32 v[12:13], v73 offset0:66 offset1:82
	ds_read2_b32 v[14:15], v73 offset0:99 offset1:115
	ds_read2_b32 v[16:17], v73 offset0:132 offset1:148
	ds_read2_b32 v[18:19], v73 offset0:165 offset1:181
	ds_read2_b32 v[20:21], v73 offset0:198 offset1:214
	ds_read2_b32 v[22:23], v73 offset0:231 offset1:247
	ds_read2_b32 v[24:25], v5 offset0:8 offset1:24
	ds_read2_b32 v[26:27], v5 offset0:41 offset1:57
	ds_read2_b32 v[28:29], v5 offset0:74 offset1:90
	ds_read2_b32 v[30:31], v5 offset0:107 offset1:123
	ds_read2_b32 v[32:33], v5 offset0:140 offset1:156
	ds_read2_b32 v[68:69], v5 offset0:173 offset1:189
	v_mov_b32_e32 v2, 0
	v_mov_b32_e32 v3, 0
	v_mov_b32_e32 v4, 0
	ds_read2_b32 v[76:77], v5 offset0:206 offset1:222
	ds_read2_b32 v[78:79], v5 offset0:239 offset1:255
	v_mov_b32_e32 v5, 0
	s_waitcnt lgkmcnt(14)
	v_cvt_pk_fp8_f32 v2, v8, v10
	s_waitcnt lgkmcnt(10)
	v_cvt_pk_fp8_f32 v3, v16, v18
	s_waitcnt lgkmcnt(6)
	v_cvt_pk_fp8_f32 v4, v24, v26
	s_waitcnt lgkmcnt(2)
	v_cvt_pk_fp8_f32 v5, v32, v68
	s_ashr_i32 s5, s19, 31
	s_add_u32 s6, s6, s19
	v_cvt_pk_fp8_f32 v2, v12, v14 op_sel:[0,0,1]
	v_cvt_pk_fp8_f32 v3, v20, v22 op_sel:[0,0,1]
	v_cvt_pk_fp8_f32 v4, v28, v30 op_sel:[0,0,1]
	s_waitcnt lgkmcnt(0)
	v_cvt_pk_fp8_f32 v5, v76, v78 op_sel:[0,0,1]
	s_addc_u32 s7, s7, s5
	v_lshl_add_u64 v[6:7], s[6:7], 0, v[66:67]
	v_add_u32_e32 v8, s9, v72
	v_mad_i64_i32 v[80:81], s[6:7], s4, v8, v[6:7]
	global_store_dwordx4 v[80:81], v[2:5], off
	v_add_u32_e32 v8, s9, v74
	v_mad_i64_i32 v[6:7], s[4:5], s4, v8, v[6:7]
	v_mov_b32_e32 v2, 0
	v_mov_b32_e32 v3, 0
	v_mov_b32_e32 v4, 0
	v_mov_b32_e32 v5, 0
	v_cvt_pk_fp8_f32 v2, v9, v11
	v_cvt_pk_fp8_f32 v3, v17, v19
	v_cvt_pk_fp8_f32 v4, v25, v27
	v_cvt_pk_fp8_f32 v5, v33, v69
	v_cvt_pk_fp8_f32 v2, v13, v15 op_sel:[0,0,1]
	v_cvt_pk_fp8_f32 v3, v21, v23 op_sel:[0,0,1]
	v_cvt_pk_fp8_f32 v4, v29, v31 op_sel:[0,0,1]
	v_cvt_pk_fp8_f32 v5, v77, v79 op_sel:[0,0,1]
	s_add_i32 s14, s14, s15
	s_add_i32 s16, s16, s17
	s_andn2_b64 vcc, exec, s[0:1]
	global_store_dwordx4 v[6:7], v[2:5], off
	s_waitcnt vmcnt(2) lgkmcnt(0)
	s_mov_b32 s9, s18
	v_mov_b32_e32 v6, v42
	v_mov_b32_e32 v2, v38
	v_mov_b32_e32 v3, v39
	v_mov_b32_e32 v4, v40
	v_mov_b32_e32 v5, v41
	v_mov_b32_e32 v7, v43
	v_mov_b32_e32 v8, v44
	v_mov_b32_e32 v9, v45
	v_mov_b32_e32 v10, v34
	v_mov_b32_e32 v11, v35
	v_mov_b32_e32 v12, v36
	v_mov_b32_e32 v13, v37
	v_mov_b32_e32 v14, v46
	v_mov_b32_e32 v15, v47
	v_mov_b32_e32 v16, v48
	v_mov_b32_e32 v17, v49
	v_mov_b32_e32 v18, v54
	v_mov_b32_e32 v19, v55
	v_mov_b32_e32 v20, v56
	v_mov_b32_e32 v21, v57
	v_mov_b32_e32 v22, v58
	v_mov_b32_e32 v23, v59
	v_mov_b32_e32 v24, v60
	v_mov_b32_e32 v25, v61
	v_mov_b32_e32 v26, v50
	v_mov_b32_e32 v27, v51
	v_mov_b32_e32 v28, v52
	v_mov_b32_e32 v29, v53
	v_mov_b32_e32 v30, v62
	v_mov_b32_e32 v31, v63
	v_mov_b32_e32 v32, v64
	v_mov_b32_e32 v33, v65
	s_cbranch_vccz .LBB0_95

.LBB0_2425:
	s_waitcnt vmcnt(8)
	s_andn2_b64 vcc, exec, s[8:9]
	s_cbranch_vccnz .Lcf_hnb
	s_waitcnt vmcnt(0)
.Lcf_hnb:
	v_pk_mul_f32 v[8:9], v[8:9], s[18:19] op_sel_hi:[1,0]
	ds_write2_b32 v74, v8, v9 offset1:1
	v_pk_mul_f32 v[8:9], v[10:11], s[18:19] op_sel_hi:[1,0]
	ds_write2_b32 v74, v8, v9 offset0:2 offset1:3
	v_pk_mul_f32 v[4:5], v[4:5], s[18:19] op_sel_hi:[1,0]
	v_add_u32_e32 v8, 0x420, v74
	ds_write2_b32 v8, v4, v5 offset1:1
	v_pk_mul_f32 v[4:5], v[6:7], s[18:19] op_sel_hi:[1,0]
	v_add_u32_e32 v6, 0x428, v74
	ds_write2_b32 v6, v4, v5 offset1:1
	v_pk_mul_f32 v[4:5], v[16:17], s[18:19] op_sel_hi:[1,0]
	v_add_u32_e32 v6, 0x840, v74
	ds_write2_b32 v6, v4, v5 offset1:1
	v_pk_mul_f32 v[4:5], v[18:19], s[18:19] op_sel_hi:[1,0]
	v_add_u32_e32 v6, 0x848, v74
	ds_write2_b32 v6, v4, v5 offset1:1
	v_pk_mul_f32 v[4:5], v[12:13], s[18:19] op_sel_hi:[1,0]
	v_add_u32_e32 v6, 0xc60, v74
	ds_write2_b32 v6, v4, v5 offset1:1
	v_pk_mul_f32 v[4:5], v[14:15], s[18:19] op_sel_hi:[1,0]
	v_add_u32_e32 v6, 0xc68, v74
	ds_write2_b32 v6, v4, v5 offset1:1
	v_pk_mul_f32 v[4:5], v[24:25], s[18:19] op_sel_hi:[1,0]
	v_add_u32_e32 v6, 0x1080, v74
	ds_write2_b32 v6, v4, v5 offset1:1
	v_pk_mul_f32 v[4:5], v[26:27], s[18:19] op_sel_hi:[1,0]
	v_add_u32_e32 v6, 0x1088, v74
	ds_write2_b32 v6, v4, v5 offset1:1
	v_pk_mul_f32 v[4:5], v[20:21], s[18:19] op_sel_hi:[1,0]
	v_add_u32_e32 v6, 0x14a0, v74
	ds_write2_b32 v6, v4, v5 offset1:1
	v_pk_mul_f32 v[4:5], v[22:23], s[18:19] op_sel_hi:[1,0]
	v_add_u32_e32 v6, 0x14a8, v74
	ds_write2_b32 v6, v4, v5 offset1:1
	v_pk_mul_f32 v[4:5], v[32:33], s[18:19] op_sel_hi:[1,0]
	v_add_u32_e32 v6, 0x18c0, v74
	ds_write2_b32 v6, v4, v5 offset1:1
	v_pk_mul_f32 v[4:5], v[34:35], s[18:19] op_sel_hi:[1,0]
	v_add_u32_e32 v6, 0x18c8, v74
	ds_write2_b32 v6, v4, v5 offset1:1
	v_pk_mul_f32 v[4:5], v[28:29], s[18:19] op_sel_hi:[1,0]
	v_add_u32_e32 v6, 0x1ce0, v74
	ds_write2_b32 v6, v4, v5 offset1:1
	v_pk_mul_f32 v[4:5], v[30:31], s[18:19] op_sel_hi:[1,0]
	v_add_u32_e32 v6, 0x1ce8, v74
	ds_write2_b32 v6, v4, v5 offset1:1
	s_waitcnt lgkmcnt(0)
	v_add_u32_e32 v7, 0x400, v72
	ds_read2_b32 v[10:11], v72 offset1:16
	ds_read2_b32 v[12:13], v72 offset0:33 offset1:49
	ds_read2_b32 v[14:15], v72 offset0:66 offset1:82
	ds_read2_b32 v[16:17], v72 offset0:99 offset1:115
	ds_read2_b32 v[18:19], v72 offset0:132 offset1:148
	ds_read2_b32 v[20:21], v72 offset0:165 offset1:181
	ds_read2_b32 v[22:23], v72 offset0:198 offset1:214
	ds_read2_b32 v[24:25], v72 offset0:231 offset1:247
	ds_read2_b32 v[26:27], v7 offset0:8 offset1:24
	ds_read2_b32 v[28:29], v7 offset0:41 offset1:57
	ds_read2_b32 v[30:31], v7 offset0:74 offset1:90
	ds_read2_b32 v[32:33], v7 offset0:107 offset1:123
	ds_read2_b32 v[34:35], v7 offset0:140 offset1:156
	ds_read2_b32 v[68:69], v7 offset0:173 offset1:189
	v_mov_b32_e32 v4, v3
	v_mov_b32_e32 v5, v3
	v_mov_b32_e32 v6, v3
	ds_read2_b32 v[76:77], v7 offset0:206 offset1:222
	ds_read2_b32 v[78:79], v7 offset0:239 offset1:255
	v_mov_b32_e32 v7, v3
	s_waitcnt lgkmcnt(14)
	v_cvt_pk_fp8_f32 v4, v10, v12
	s_waitcnt lgkmcnt(10)
	v_cvt_pk_fp8_f32 v5, v18, v20
	s_waitcnt lgkmcnt(6)
	v_cvt_pk_fp8_f32 v6, v26, v28
	s_waitcnt lgkmcnt(2)
	v_cvt_pk_fp8_f32 v7, v34, v68
	s_ashr_i32 s1, s30, 31
	s_add_u32 s0, s16, s30
	v_cvt_pk_fp8_f32 v4, v14, v16 op_sel:[0,0,1]
	v_cvt_pk_fp8_f32 v5, v22, v24 op_sel:[0,0,1]
	v_cvt_pk_fp8_f32 v6, v30, v32 op_sel:[0,0,1]
	s_waitcnt lgkmcnt(0)
	v_cvt_pk_fp8_f32 v7, v76, v78 op_sel:[0,0,1]
	s_addc_u32 s1, s17, s1
	v_lshl_add_u64 v[8:9], s[0:1], 0, v[2:3]
	v_add_u32_e32 v10, s29, v71
	v_mad_i64_i32 v[80:81], s[0:1], s14, v10, v[8:9]
	global_store_dwordx4 v[80:81], v[4:7], off
	v_add_u32_e32 v10, s29, v73
	v_mad_i64_i32 v[8:9], s[0:1], s14, v10, v[8:9]
	v_mov_b32_e32 v4, v3
	v_mov_b32_e32 v5, v3
	v_mov_b32_e32 v6, v3
	v_mov_b32_e32 v7, v3
	v_cvt_pk_fp8_f32 v4, v11, v13
	v_cvt_pk_fp8_f32 v5, v19, v21
	v_cvt_pk_fp8_f32 v6, v27, v29
	v_cvt_pk_fp8_f32 v7, v35, v69
	v_cvt_pk_fp8_f32 v4, v15, v17 op_sel:[0,0,1]
	v_cvt_pk_fp8_f32 v5, v23, v25 op_sel:[0,0,1]
	v_cvt_pk_fp8_f32 v6, v31, v33 op_sel:[0,0,1]
	v_cvt_pk_fp8_f32 v7, v77, v79 op_sel:[0,0,1]
	s_add_i32 s24, s24, s25
	s_add_i32 s26, s26, s27
	s_andn2_b64 vcc, exec, s[8:9]
	global_store_dwordx4 v[8:9], v[4:7], off
	s_waitcnt vmcnt(2) lgkmcnt(0)
	s_mov_b32 s16, s28
	v_mov_b32_e32 v8, v40
	v_mov_b32_e32 v9, v41
	v_mov_b32_e32 v10, v42
	v_mov_b32_e32 v11, v43
	v_mov_b32_e32 v4, v44
	v_mov_b32_e32 v5, v45
	v_mov_b32_e32 v6, v46
	v_mov_b32_e32 v7, v47
	v_mov_b32_e32 v16, v36
	v_mov_b32_e32 v17, v37
	v_mov_b32_e32 v18, v38
	v_mov_b32_e32 v19, v39
	v_mov_b32_e32 v12, v48
	v_mov_b32_e32 v13, v49
	v_mov_b32_e32 v14, v50
	v_mov_b32_e32 v15, v51
	v_mov_b32_e32 v24, v56
	v_mov_b32_e32 v25, v57
	v_mov_b32_e32 v26, v58
	v_mov_b32_e32 v27, v59
	v_mov_b32_e32 v20, v60
	v_mov_b32_e32 v21, v61
	v_mov_b32_e32 v22, v62
	v_mov_b32_e32 v23, v63
	v_mov_b32_e32 v32, v52
	v_mov_b32_e32 v33, v53
	v_mov_b32_e32 v34, v54
	v_mov_b32_e32 v35, v55
	v_mov_b32_e32 v28, v64
	v_mov_b32_e32 v29, v65
	v_mov_b32_e32 v30, v66
	v_mov_b32_e32 v31, v67
	s_cbranch_vccz .LBB0_2474
